# baseline (speedup 1.0000x reference)
.LBB1_12:
	s_mov_b32 s0, s44
	s_add_i32 s44, s44, 1
	s_cmp_ge_u32 s44, s42
	s_cselect_b64 s[22:23], -1, 0
	s_cmp_lt_u32 s44, s42
	s_cselect_b32 s2, s44, s0
	s_waitcnt vmcnt(0)
	s_lshl_b32 s0, s2, 4
	s_mov_b32 s1, s17
	s_mov_b32 m0, s43
	ds_read_b128 v[76:79], v119 offset:32768
	ds_read_b128 v[80:83], v119 offset:36864
	ds_read_b128 v[84:87], v120 offset:32768
	ds_read_b128 v[88:91], v120 offset:36864
	ds_read_b128 v[92:95], v121
	ds_read_b128 v[96:99], v121 offset:4096
	ds_read_b128 v[128:131], v122
	ds_read_b128 v[132:135], v122 offset:4096
	ds_read_b128 v[72:75], v123
	s_waitcnt lgkmcnt(0)
	v_lshl_add_u64 v[70:71], s[0:1], 2, v[2:3]
	global_load_lds_dword v[70:71], off
	ds_read_b128 v[156:159], v115
	ds_read_b128 v[160:163], v115 offset:1024
	ds_read_b128 v[164:167], v115 offset:2048
	v_cvt_pk_bf16_f32 v136, v76, v77
	v_cvt_pk_bf16_f32 v137, v78, v79
	v_cvt_pk_bf16_f32 v138, v84, v85
	v_cvt_pk_bf16_f32 v139, v86, v87
	v_cvt_pk_bf16_f32 v140, v92, v93
	v_cvt_pk_bf16_f32 v141, v94, v95
	v_cvt_pk_bf16_f32 v142, v128, v129
	v_cvt_pk_bf16_f32 v143, v130, v131
	v_cvt_pk_bf16_f32 v144, v80, v81
	v_cvt_pk_bf16_f32 v145, v82, v83
	v_cvt_pk_bf16_f32 v146, v88, v89
	v_cvt_pk_bf16_f32 v147, v90, v91
	v_cvt_pk_bf16_f32 v128, v96, v97
	v_cvt_pk_bf16_f32 v129, v98, v99
	v_cvt_pk_bf16_f32 v130, v132, v133
	v_cvt_pk_bf16_f32 v131, v134, v135
	s_lshl_b32 s0, s2, 13
	s_cmp_lt_u32 s44, s42
	s_cselect_b32 s0, s0, 0x1e848000
	ds_read_b128 v[132:135], v115 offset:3072
	s_waitcnt lgkmcnt(3)
	v_mfma_f32_16x16x32_bf16 v[148:151], v[136:139], v[156:159], v[36:39]
	ds_read_b128 v[156:159], v115 offset:4096
	s_waitcnt lgkmcnt(3)
	v_mfma_f32_16x16x32_bf16 v[152:155], v[136:139], v[160:163], v[40:43]
	ds_read_b128 v[160:163], v115 offset:5120
	s_waitcnt lgkmcnt(3)
	v_mfma_f32_16x16x32_bf16 v[96:99], v[136:139], v[164:167], v[44:47]
	ds_read_b128 v[164:167], v115 offset:6144
	s_waitcnt lgkmcnt(3)
	v_mfma_f32_16x16x32_bf16 v[92:95], v[136:139], v[132:135], v[48:51]
	s_mov_b32 m0, s47
	s_nop 0
	buffer_load_dwordx4 v113, s[12:15], s0 offen nt lds
	ds_read_b128 v[132:135], v115 offset:7168
	s_waitcnt lgkmcnt(3)
	v_mfma_f32_16x16x32_bf16 v[88:91], v[136:139], v[156:159], v[52:55]
	ds_read_b128 v[156:159], v115 offset:8192
	s_waitcnt lgkmcnt(3)
	v_mfma_f32_16x16x32_bf16 v[84:87], v[136:139], v[160:163], v[56:59]
	ds_read_b128 v[160:163], v115 offset:9216
	s_waitcnt lgkmcnt(3)
	v_mfma_f32_16x16x32_bf16 v[80:83], v[136:139], v[164:167], v[60:63]
	ds_read_b128 v[164:167], v115 offset:10240
	s_waitcnt lgkmcnt(3)
	v_mfma_f32_16x16x32_bf16 v[76:79], v[136:139], v[132:135], v[64:67]
	s_or_b32 s1, s0, 0x800
	s_mov_b32 m0, s48
	s_nop 0
	buffer_load_dwordx4 v113, s[12:15], s1 offen nt lds
	ds_read_b128 v[132:135], v115 offset:11264
	s_waitcnt lgkmcnt(3)
	v_mfma_f32_16x16x32_bf16 v[148:151], v[140:143], v[156:159], v[148:151]
	ds_read_b128 v[156:159], v115 offset:12288
	s_waitcnt lgkmcnt(3)
	v_mfma_f32_16x16x32_bf16 v[152:155], v[140:143], v[160:163], v[152:155]
	ds_read_b128 v[160:163], v115 offset:13312
	s_waitcnt lgkmcnt(3)
	v_mfma_f32_16x16x32_bf16 v[96:99], v[140:143], v[164:167], v[96:99]
	ds_read_b128 v[164:167], v115 offset:14336
	s_waitcnt lgkmcnt(3)
	v_mfma_f32_16x16x32_bf16 v[92:95], v[140:143], v[132:135], v[92:95]
	s_or_b32 s1, s0, 0x1000
	s_mov_b32 m0, s49
	s_nop 0
	buffer_load_dwordx4 v113, s[12:15], s1 offen nt lds
	ds_read_b128 v[132:135], v115 offset:15360
	s_waitcnt lgkmcnt(3)
	v_mfma_f32_16x16x32_bf16 v[88:91], v[140:143], v[156:159], v[88:91]
	ds_read_b128 v[156:159], v115 offset:16384
	s_waitcnt lgkmcnt(3)
	v_mfma_f32_16x16x32_bf16 v[84:87], v[140:143], v[160:163], v[84:87]
	ds_read_b128 v[160:163], v115 offset:17408
	s_waitcnt lgkmcnt(3)
	v_mfma_f32_16x16x32_bf16 v[80:83], v[140:143], v[164:167], v[80:83]
	ds_read_b128 v[164:167], v115 offset:18432
	s_waitcnt lgkmcnt(3)
	v_mfma_f32_16x16x32_bf16 v[76:79], v[140:143], v[132:135], v[76:79]
	s_or_b32 s1, s0, 0x1800
	s_mov_b32 m0, s50
	s_nop 0
	buffer_load_dwordx4 v113, s[12:15], s1 offen nt lds
	ds_read_b128 v[132:135], v115 offset:19456
	s_waitcnt lgkmcnt(3)
	v_mfma_f32_16x16x32_bf16 v[148:151], v[144:147], v[156:159], v[148:151]
	ds_read_b128 v[156:159], v115 offset:20480
	s_waitcnt lgkmcnt(3)
	v_mfma_f32_16x16x32_bf16 v[152:155], v[144:147], v[160:163], v[152:155]
	ds_read_b128 v[160:163], v115 offset:21504
	s_waitcnt lgkmcnt(3)
	v_mfma_f32_16x16x32_bf16 v[96:99], v[144:147], v[164:167], v[96:99]
	ds_read_b128 v[164:167], v115 offset:22528
	s_waitcnt lgkmcnt(3)
	v_mfma_f32_16x16x32_bf16 v[92:95], v[144:147], v[132:135], v[92:95]
	s_or_b32 s1, s0, 0x100
	s_mov_b32 m0, s51
	s_nop 0
	buffer_load_dwordx4 v113, s[12:15], s1 offen nt lds
	ds_read_b128 v[132:135], v115 offset:23552
	s_waitcnt lgkmcnt(3)
	v_mfma_f32_16x16x32_bf16 v[88:91], v[144:147], v[156:159], v[88:91]
	ds_read_b128 v[156:159], v115 offset:24576
	s_waitcnt lgkmcnt(3)
	v_mfma_f32_16x16x32_bf16 v[84:87], v[144:147], v[160:163], v[84:87]
	ds_read_b128 v[160:163], v115 offset:25600
	s_waitcnt lgkmcnt(3)
	v_mfma_f32_16x16x32_bf16 v[80:83], v[144:147], v[164:167], v[80:83]
	ds_read_b128 v[164:167], v115 offset:26624
	s_waitcnt lgkmcnt(3)
	v_mfma_f32_16x16x32_bf16 v[76:79], v[144:147], v[132:135], v[76:79]
	s_or_b32 s1, s0, 0x900
	s_mov_b32 m0, s52
	s_nop 0
	buffer_load_dwordx4 v113, s[12:15], s1 offen nt lds
	ds_read_b128 v[132:135], v115 offset:27648
	s_waitcnt lgkmcnt(3)
	v_mfma_f32_16x16x32_bf16 v[148:151], v[128:131], v[156:159], v[148:151]
	ds_read_b128 v[156:159], v115 offset:28672
	s_waitcnt lgkmcnt(3)
	v_mfma_f32_16x16x32_bf16 v[152:155], v[128:131], v[160:163], v[152:155]
	ds_read_b128 v[160:163], v115 offset:29696
	s_waitcnt lgkmcnt(3)
	v_mfma_f32_16x16x32_bf16 v[96:99], v[128:131], v[164:167], v[96:99]
	ds_read_b128 v[164:167], v115 offset:30720
	s_waitcnt lgkmcnt(3)
	v_mfma_f32_16x16x32_bf16 v[92:95], v[128:131], v[132:135], v[92:95]
	s_or_b32 s1, s0, 0x1100
	s_mov_b32 m0, s53
	s_nop 0
	buffer_load_dwordx4 v113, s[12:15], s1 offen nt lds
	ds_read_b128 v[132:135], v115 offset:31744
	s_waitcnt lgkmcnt(3)
	v_mfma_f32_16x16x32_bf16 v[88:91], v[128:131], v[156:159], v[88:91]
	s_waitcnt lgkmcnt(2)
	v_mfma_f32_16x16x32_bf16 v[84:87], v[128:131], v[160:163], v[84:87]
	s_waitcnt lgkmcnt(1)
	v_mfma_f32_16x16x32_bf16 v[80:83], v[128:131], v[164:167], v[80:83]
	s_waitcnt lgkmcnt(0)
	v_mfma_f32_16x16x32_bf16 v[76:79], v[128:131], v[132:135], v[76:79]
	s_or_b32 s1, s0, 0x1900
	s_mov_b32 m0, s54
	s_nop 0
	buffer_load_dwordx4 v113, s[12:15], s1 offen nt lds
	ds_read2_b32 v[136:137], v114 offset0:128 offset1:144
	ds_read2_b32 v[138:139], v125 offset1:16
	ds_read2_b32 v[140:141], v114 offset0:160 offset1:176
	ds_read2_b32 v[142:143], v125 offset0:32 offset1:48
	ds_read2_b32 v[144:145], v114 offset0:192 offset1:208
	ds_read2_b32 v[146:147], v125 offset0:64 offset1:80
	ds_read2_b32 v[156:157], v114 offset0:224 offset1:240
	ds_read2_b32 v[158:159], v125 offset0:96 offset1:112
	v_fma_f32 v70, v149, v149, 0
	v_fmac_f32_e32 v70, v153, v153
	v_fmac_f32_e32 v70, v97, v97
	v_fmac_f32_e32 v70, v93, v93
	v_fmac_f32_e32 v70, v89, v89
	v_fmac_f32_e32 v70, v85, v85
	v_fmac_f32_e32 v70, v81, v81
	v_fmac_f32_e32 v70, v77, v77
	v_fma_f32 v68, v148, v148, 0
	v_fmac_f32_e32 v68, v152, v152
	v_add_f32_dpp v70, v70, v70 quad_perm:[1,0,3,2] row_mask:0xf bank_mask:0xf bound_ctrl:1
	v_fmac_f32_e32 v68, v96, v96
	v_fmac_f32_e32 v68, v92, v92
	v_add_f32_dpp v70, v70, v70 quad_perm:[2,3,0,1] row_mask:0xf bank_mask:0xf bound_ctrl:1
	v_fmac_f32_e32 v68, v88, v88
	v_fmac_f32_e32 v68, v84, v84
	v_add_f32_dpp v70, v70, v70 row_half_mirror row_mask:0xf bank_mask:0xf bound_ctrl:1
	v_fmac_f32_e32 v68, v80, v80
	v_fmac_f32_e32 v68, v76, v76
	v_add_f32_dpp v70, v70, v70 row_mirror row_mask:0xf bank_mask:0xf bound_ctrl:1
	v_fmamk_f32 v70, v70, 0x3c000000, v124
	v_rsq_f32_e32 v127, v70
	v_fma_f32 v70, v150, v150, 0
	v_fmac_f32_e32 v70, v154, v154
	v_fmac_f32_e32 v70, v98, v98
	v_fmac_f32_e32 v70, v94, v94
	v_fmac_f32_e32 v70, v90, v90
	v_fmac_f32_e32 v70, v86, v86
	v_fmac_f32_e32 v70, v82, v82
	v_fmac_f32_e32 v70, v78, v78
	v_add_f32_dpp v68, v68, v68 quad_perm:[1,0,3,2] row_mask:0xf bank_mask:0xf bound_ctrl:1
	v_mul_f32_e32 v131, v127, v149
	v_add_f32_dpp v70, v70, v70 quad_perm:[1,0,3,2] row_mask:0xf bank_mask:0xf bound_ctrl:1
	v_add_f32_dpp v68, v68, v68 quad_perm:[2,3,0,1] row_mask:0xf bank_mask:0xf bound_ctrl:1
	v_mul_f32_e32 v81, v127, v81
	v_add_f32_dpp v70, v70, v70 quad_perm:[2,3,0,1] row_mask:0xf bank_mask:0xf bound_ctrl:1
	v_add_f32_dpp v68, v68, v68 row_half_mirror row_mask:0xf bank_mask:0xf bound_ctrl:1
	v_cmp_gt_u32_e64 s[0:1], s55, v72
	v_add_f32_dpp v70, v70, v70 row_half_mirror row_mask:0xf bank_mask:0xf bound_ctrl:1
	v_add_f32_dpp v68, v68, v68 row_mirror row_mask:0xf bank_mask:0xf bound_ctrl:1
	v_fmamk_f32 v68, v68, 0x3c000000, v124
	v_add_f32_dpp v70, v70, v70 row_mirror row_mask:0xf bank_mask:0xf bound_ctrl:1
	v_fmamk_f32 v70, v70, 0x3c000000, v124
	v_rsq_f32_e32 v130, v70
	v_fma_f32 v70, v151, v151, 0
	v_fmac_f32_e32 v70, v155, v155
	v_fmac_f32_e32 v70, v99, v99
	v_fmac_f32_e32 v70, v95, v95
	v_fmac_f32_e32 v70, v91, v91
	v_fmac_f32_e32 v70, v87, v87
	v_fmac_f32_e32 v70, v83, v83
	v_fmac_f32_e32 v70, v79, v79
	v_rsq_f32_e32 v68, v68
	v_mul_f32_e32 v98, v130, v98
	v_add_f32_dpp v70, v70, v70 quad_perm:[1,0,3,2] row_mask:0xf bank_mask:0xf bound_ctrl:1
	v_mul_f32_e32 v90, v130, v90
	v_mul_f32_e32 v111, v68, v148
	v_add_f32_dpp v110, v70, v70 quad_perm:[2,3,0,1] row_mask:0xf bank_mask:0xf bound_ctrl:1
	s_nop 1
	v_add_f32_dpp v110, v110, v110 row_half_mirror row_mask:0xf bank_mask:0xf bound_ctrl:1
	v_mul_f32_e32 v96, v68, v96
	v_mul_f32_e32 v92, v68, v92
	v_add_f32_dpp v110, v110, v110 row_mirror row_mask:0xf bank_mask:0xf bound_ctrl:1
	v_fmamk_f32 v110, v110, 0x3c000000, v124
	s_waitcnt lgkmcnt(0)
	v_fma_f32 v111, v111, v136, v138
	v_fma_f32 v131, v131, v136, v138
	v_exp_f32_e32 v111, v111
	v_exp_f32_e32 v131, v131
	v_rsq_f32_e32 v132, v110
	v_mul_f32_e32 v88, v68, v88
	v_add_f32_e32 v110, 1.0, v111
	v_add_f32_e32 v111, 1.0, v131
	v_mul_f32_e32 v131, v130, v150
	v_mul_f32_e32 v133, v132, v151
	v_fma_f32 v131, v131, v136, v138
	v_fma_f32 v70, v133, v136, v138
	v_exp_f32_e32 v131, v131
	v_exp_f32_e32 v70, v70
	v_rcp_f32_e32 v110, v110
	v_rcp_f32_e32 v111, v111
	v_add_f32_e32 v128, 1.0, v131
	v_add_f32_e32 v70, 1.0, v70
	v_rcp_f32_e32 v128, v128
	v_rcp_f32_e32 v70, v70
	v_mul_f32_e32 v131, v68, v152
	v_fma_f32 v131, v131, v137, v139
	v_cvt_pk_bf16_f32 v110, v110, v111
	v_cvt_pk_bf16_f32 v111, v128, v70
	v_mul_f32_e32 v128, v127, v153
	v_exp_f32_e32 v131, v131
	v_fma_f32 v128, v128, v137, v139
	v_exp_f32_e32 v128, v128
	v_mul_f32_e32 v99, v132, v99
	v_add_f32_e32 v70, 1.0, v131
	v_rcp_f32_e32 v133, v70
	v_add_f32_e32 v70, 1.0, v128
	v_mul_f32_e32 v131, v130, v154
	v_rcp_f32_e32 v134, v70
	v_mul_f32_e32 v70, v132, v155
	v_fma_f32 v131, v131, v137, v139
	v_fma_f32 v129, v70, v137, v139
	v_exp_f32_e32 v135, v129
	v_exp_f32_e32 v131, v131
	v_mul_f32_e32 v91, v132, v91
	v_add_f32_e32 v135, 1.0, v135
	v_rcp_f32_e32 v135, v135
	v_fma_f32 v96, v96, v140, v142
	v_exp_f32_e32 v136, v96
	v_mul_f32_e32 v96, v127, v97
	v_fma_f32 v96, v96, v140, v142
	v_exp_f32_e32 v97, v96
	v_fma_f32 v98, v98, v140, v142
	v_fma_f32 v70, v99, v140, v142
	v_exp_f32_e32 v98, v98
	v_exp_f32_e32 v70, v70
	v_add_f32_e32 v97, 1.0, v97
	v_cvt_pk_bf16_f32 v96, v133, v134
	v_add_f32_e32 v133, 1.0, v136
	v_rcp_f32_e32 v99, v97
	v_add_f32_e32 v97, 1.0, v98
	v_add_f32_e32 v70, 1.0, v70
	v_fma_f32 v92, v92, v141, v143
	v_rcp_f32_e32 v133, v133
	v_rcp_f32_e32 v128, v97
	v_rcp_f32_e32 v70, v70
	v_exp_f32_e32 v92, v92
	v_cvt_pk_bf16_f32 v98, v133, v99
	v_add_f32_e32 v131, 1.0, v131
	v_cvt_pk_bf16_f32 v99, v128, v70
	v_add_f32_e32 v70, 1.0, v92
	v_mul_f32_e32 v92, v127, v93
	v_fma_f32 v92, v92, v141, v143
	v_exp_f32_e32 v92, v92
	v_mul_f32_e32 v93, v130, v94
	v_fma_f32 v93, v93, v141, v143
	v_rcp_f32_e32 v131, v131
	v_exp_f32_e32 v93, v93
	v_rcp_f32_e32 v94, v70
	v_add_f32_e32 v70, 1.0, v92
	v_rcp_f32_e32 v128, v70
	v_mul_f32_e32 v70, v132, v95
	v_cvt_pk_bf16_f32 v97, v131, v135
	v_add_f32_e32 v131, 1.0, v93
	v_fma_f32 v129, v70, v141, v143
	v_exp_f32_e32 v95, v129
	v_rcp_f32_e32 v129, v131
	v_mul_f32_e32 v84, v68, v84
	v_mul_f32_e32 v80, v68, v80
	v_fma_f32 v88, v88, v144, v146
	v_exp_f32_e32 v131, v88
	v_mul_f32_e32 v88, v127, v89
	v_fma_f32 v88, v88, v144, v146
	v_exp_f32_e32 v89, v88
	v_fma_f32 v90, v90, v144, v146
	v_fma_f32 v70, v91, v144, v146
	v_exp_f32_e32 v90, v90
	v_exp_f32_e32 v70, v70
	v_add_f32_e32 v89, 1.0, v89
	v_cvt_pk_bf16_f32 v88, v94, v128
	v_add_f32_e32 v94, 1.0, v131
	v_rcp_f32_e32 v91, v89
	v_add_f32_e32 v89, 1.0, v90
	v_add_f32_e32 v70, 1.0, v70
	v_fma_f32 v84, v84, v145, v147
	v_rcp_f32_e32 v94, v94
	v_rcp_f32_e32 v92, v89
	v_rcp_f32_e32 v70, v70
	v_exp_f32_e32 v84, v84
	v_cvt_pk_bf16_f32 v90, v94, v91
	v_mul_f32_e32 v68, v68, v76
	v_cvt_pk_bf16_f32 v91, v92, v70
	v_add_f32_e32 v70, 1.0, v84
	v_mul_f32_e32 v84, v127, v85
	v_fma_f32 v84, v84, v145, v147
	v_mul_f32_e32 v85, v130, v86
	v_exp_f32_e32 v84, v84
	v_fma_f32 v85, v85, v145, v147
	v_exp_f32_e32 v85, v85
	v_rcp_f32_e32 v92, v70
	v_add_f32_e32 v70, 1.0, v84
	v_rcp_f32_e32 v84, v70
	v_add_f32_e32 v70, 1.0, v85
	v_mul_f32_e32 v85, v132, v87
	v_fma_f32 v93, v85, v145, v147
	v_exp_f32_e32 v85, v93
	v_rcp_f32_e32 v93, v70
	v_mul_f32_e32 v76, v127, v77
	v_mul_f32_e32 v82, v130, v82
	v_mul_f32_e32 v83, v132, v83
	v_mul_f32_e32 v77, v130, v78
	v_fma_f32 v76, v76, v157, v159
	v_mul_f32_e32 v78, v132, v79
	v_fma_f32 v80, v80, v156, v158
	v_fma_f32 v81, v81, v156, v158
	v_fma_f32 v82, v82, v156, v158
	v_fma_f32 v70, v83, v156, v158
	v_fma_f32 v68, v68, v157, v159
	v_exp_f32_e32 v76, v76
	v_fma_f32 v77, v77, v157, v159
	v_fma_f32 v87, v78, v157, v159
	v_exp_f32_e32 v82, v82
	v_exp_f32_e32 v70, v70
	v_exp_f32_e32 v68, v68
	v_exp_f32_e32 v77, v77
	v_exp_f32_e32 v71, v87
	v_add_f32_e32 v76, 1.0, v76
	v_add_f32_e32 v82, 1.0, v82
	v_add_f32_e32 v70, 1.0, v70
	v_add_f32_e32 v68, 1.0, v68
	v_rcp_f32_e32 v78, v76
	v_add_f32_e32 v76, 1.0, v77
	v_add_f32_e32 v71, 1.0, v71
	v_rcp_f32_e32 v82, v82
	v_rcp_f32_e32 v70, v70
	v_rcp_f32_e32 v68, v68
	v_rcp_f32_e32 v79, v76
	v_rcp_f32_e32 v71, v71
	v_exp_f32_e32 v80, v80
	v_exp_f32_e32 v81, v81
	v_cvt_pk_bf16_f32 v77, v82, v70
	v_cvt_pk_bf16_f32 v78, v68, v78
	v_cvt_pk_bf16_f32 v79, v79, v71
	v_subrev_u32_e32 v68, s16, v72
	v_subrev_u32_e32 v70, s16, v73
	v_subrev_u32_e32 v71, s16, v74
	v_add_f32_e32 v95, 1.0, v95
	v_add_f32_e32 v85, 1.0, v85
	v_add_f32_e32 v80, 1.0, v80
	v_add_f32_e32 v81, 1.0, v81
	v_max3_u32 v68, v68, v70, v71
	v_subrev_u32_e32 v70, s16, v75
	v_rcp_f32_e32 v95, v95
	v_rcp_f32_e32 v85, v85
	v_rcp_f32_e32 v80, v80
	v_rcp_f32_e32 v81, v81
	v_max_u32_e32 v68, v68, v70
	v_cmp_gt_u32_e32 vcc, 16, v68
	s_cmp_eq_u64 vcc, -1
	s_cselect_b64 s[24:25], -1, 0
	s_cmp_lg_u64 vcc, -1
	v_cvt_pk_bf16_f32 v89, v129, v95
	v_cvt_pk_bf16_f32 v84, v92, v84
	v_cvt_pk_bf16_f32 v85, v93, v85
	v_cvt_pk_bf16_f32 v76, v80, v81
	s_cselect_b64 s[26:27], -1, 0
	v_cmp_gt_u32_e64 s[2:3], s55, v73
	v_cmp_gt_u32_e64 s[4:5], s55, v74
	v_cmp_gt_u32_e64 s[6:7], s55, v75
	s_mov_b32 s8, 0
	s_branch .LBB1_14
